# baseline (speedup 1.0000x reference)
.Lchunk_loop:
	v_mfma_f32_16x16x32_f16 v[38:41], v[2:5], v[34:37], v[46:49]
	v_mfma_f32_16x16x32_f16 v[42:45], v[14:17], v[34:37], v[50:53]
	ds_read_b128 v[82:85], v94 offset:256
	ds_read_b128 v[86:89], v94 offset:272
	v_mfma_f32_16x16x32_f16 v[62:65], v[6:9], v[78:81], v[26:29]
	v_nop
	v_nop
	v_min_u32_e32 v1, v38, v40
	v_min_u32_e32 v0, v39, v41
	v_mfma_f32_16x16x32_f16 v[66:69], v[18:21], v[78:81], v[30:33]
	v_min3_u32 v1, v1, v42, v44
	v_min3_u32 v0, v0, v43, v45
	v_exp_f32_e32 v1, v1
	v_exp_f32_e32 v0, v0
	v_add_f32_e32 v1, 1.0, v1
	v_add_f32_e32 v0, 1.0, v0
	v_rcp_f32_e32 v1, v1
	v_rcp_f32_e32 v0, v0
	s_add_i32 s13, s8, 1
	v_cvt_pk_f16_f32 v34, v1, v0
	s_and_b32 s13, s13, 3
	s_mulk_i32 s13, 0x1100
	v_mov_b32_dpp v35, v34 quad_perm:[1,2,3,0] row_mask:0xf bank_mask:0xf bound_ctrl:1
	v_mov_b32_dpp v36, v34 quad_perm:[2,3,0,1] row_mask:0xf bank_mask:0xf bound_ctrl:1
	v_mov_b32_dpp v37, v34 quad_perm:[3,0,1,2] row_mask:0xf bank_mask:0xf bound_ctrl:1
	v_add_u32_e32 v95, s13, v177
	s_nop 0
	v_mfma_f32_16x16x32_f16 v[38:41], v[2:5], v[34:37], v[54:57]
	v_mfma_f32_16x16x32_f16 v[42:45], v[14:17], v[34:37], v[58:61]
	s_waitcnt lgkmcnt(0)
	v_mfma_f32_16x16x32_f16 v[70:73], v[10:13], v[78:81], v[26:29]
	v_nop
	v_nop
	v_min_u32_e32 v1, v38, v40
	v_min_u32_e32 v0, v39, v41
	v_mfma_f32_16x16x32_f16 v[74:77], v[22:25], v[78:81], v[30:33]
	v_min3_u32 v1, v1, v42, v44
	v_min3_u32 v0, v0, v43, v45
	v_exp_f32_e32 v1, v1
	v_exp_f32_e32 v0, v0
	v_add_f32_e32 v1, 1.0, v1
	v_add_f32_e32 v0, 1.0, v0
	v_rcp_f32_e32 v1, v1
	v_rcp_f32_e32 v0, v0
	v_cvt_pk_f16_f32 v78, v82, v83
	v_cvt_pk_f16_f32 v34, v1, v0
	v_cvt_pk_f16_f32 v79, v84, v85
	v_cvt_pk_f16_f32 v80, v86, v87
	v_mov_b32_dpp v35, v34 quad_perm:[1,2,3,0] row_mask:0xf bank_mask:0xf bound_ctrl:1
	v_mov_b32_dpp v36, v34 quad_perm:[2,3,0,1] row_mask:0xf bank_mask:0xf bound_ctrl:1
	v_mov_b32_dpp v37, v34 quad_perm:[3,0,1,2] row_mask:0xf bank_mask:0xf bound_ctrl:1
	v_cvt_pk_f16_f32 v81, v88, v89
	s_nop 0
	v_mfma_f32_16x16x32_f16 v[38:41], v[2:5], v[34:37], v[62:65]
	v_mfma_f32_16x16x32_f16 v[42:45], v[14:17], v[34:37], v[66:69]
	ds_read_b128 v[82:85], v94 offset:384
	ds_read_b128 v[86:89], v94 offset:400
	v_mfma_f32_16x16x32_f16 v[46:49], v[6:9], v[78:81], v[26:29]
	v_nop
	v_nop
	v_min_u32_e32 v1, v38, v40
	v_min_u32_e32 v0, v39, v41
	v_mfma_f32_16x16x32_f16 v[50:53], v[18:21], v[78:81], v[30:33]
	v_min3_u32 v1, v1, v42, v44
	v_min3_u32 v0, v0, v43, v45
	v_exp_f32_e32 v1, v1
	v_exp_f32_e32 v0, v0
	v_add_f32_e32 v1, 1.0, v1
	v_add_f32_e32 v0, 1.0, v0
	v_rcp_f32_e32 v1, v1
	v_rcp_f32_e32 v0, v0
	s_and_b32 s9, s8, 3
	v_cvt_pk_f16_f32 v34, v1, v0
	s_mulk_i32 s9, 0x1100
	s_add_i32 s9, s9, s24
	v_mov_b32_dpp v35, v34 quad_perm:[1,2,3,0] row_mask:0xf bank_mask:0xf bound_ctrl:1
	v_mov_b32_dpp v36, v34 quad_perm:[2,3,0,1] row_mask:0xf bank_mask:0xf bound_ctrl:1
	v_mov_b32_dpp v37, v34 quad_perm:[3,0,1,2] row_mask:0xf bank_mask:0xf bound_ctrl:1
	s_min_u32 s12, s8, 27
	s_lshl_b32 s22, s12, 10
	v_mfma_f32_16x16x32_f16 v[38:41], v[2:5], v[34:37], v[70:73]
	v_mfma_f32_16x16x32_f16 v[42:45], v[14:17], v[34:37], v[74:77]
	s_waitcnt lgkmcnt(0)
	v_mfma_f32_16x16x32_f16 v[54:57], v[10:13], v[78:81], v[26:29]
	v_nop
	v_nop
	v_min_u32_e32 v1, v38, v40
	v_min_u32_e32 v0, v39, v41
	v_mfma_f32_16x16x32_f16 v[58:61], v[22:25], v[78:81], v[30:33]
	v_min3_u32 v1, v1, v42, v44
	v_min3_u32 v0, v0, v43, v45
	v_exp_f32_e32 v1, v1
	v_exp_f32_e32 v0, v0
	v_add_f32_e32 v1, 1.0, v1
	v_add_f32_e32 v0, 1.0, v0
	v_rcp_f32_e32 v1, v1
	v_rcp_f32_e32 v0, v0
	v_cvt_pk_f16_f32 v78, v82, v83
	v_cvt_pk_f16_f32 v34, v1, v0
	v_cvt_pk_f16_f32 v79, v84, v85
	v_cvt_pk_f16_f32 v80, v86, v87
	v_mov_b32_dpp v35, v34 quad_perm:[1,2,3,0] row_mask:0xf bank_mask:0xf bound_ctrl:1
	v_mov_b32_dpp v36, v34 quad_perm:[2,3,0,1] row_mask:0xf bank_mask:0xf bound_ctrl:1
	v_mov_b32_dpp v37, v34 quad_perm:[3,0,1,2] row_mask:0xf bank_mask:0xf bound_ctrl:1
	v_cvt_pk_f16_f32 v81, v88, v89
	s_cmp_lt_u32 s8, 28
	s_cselect_b64 vcc, -1, 0
	v_mfma_f32_16x16x32_f16 v[38:41], v[2:5], v[34:37], v[46:49]
	v_mfma_f32_16x16x32_f16 v[42:45], v[14:17], v[34:37], v[50:53]
	ds_read_b128 v[82:85], v94 offset:512
	ds_read_b128 v[86:89], v94 offset:528
	v_mfma_f32_16x16x32_f16 v[62:65], v[6:9], v[78:81], v[26:29]
	v_nop
	v_nop
	v_min_u32_e32 v1, v38, v40
	v_min_u32_e32 v0, v39, v41
	v_mfma_f32_16x16x32_f16 v[66:69], v[18:21], v[78:81], v[30:33]
	v_min3_u32 v1, v1, v42, v44
	v_min3_u32 v0, v0, v43, v45
	v_exp_f32_e32 v1, v1
	v_exp_f32_e32 v0, v0
	v_add_f32_e32 v1, 1.0, v1
	v_add_f32_e32 v0, 1.0, v0
	v_rcp_f32_e32 v1, v1
	v_rcp_f32_e32 v0, v0
	v_lshl_add_u64 v[90:91], v[166:167], 0, s[22:23]
	v_cvt_pk_f16_f32 v34, v1, v0
	s_add_i32 s8, s8, 1
	s_nop 0
	v_mov_b32_dpp v35, v34 quad_perm:[1,2,3,0] row_mask:0xf bank_mask:0xf bound_ctrl:1
	v_mov_b32_dpp v36, v34 quad_perm:[2,3,0,1] row_mask:0xf bank_mask:0xf bound_ctrl:1
	v_mov_b32_dpp v37, v34 quad_perm:[3,0,1,2] row_mask:0xf bank_mask:0xf bound_ctrl:1
	s_nop 0
	s_nop 0
	v_mfma_f32_16x16x32_f16 v[38:41], v[2:5], v[34:37], v[54:57]
	v_mfma_f32_16x16x32_f16 v[42:45], v[14:17], v[34:37], v[58:61]
	s_waitcnt lgkmcnt(0)
	v_mfma_f32_16x16x32_f16 v[70:73], v[10:13], v[78:81], v[26:29]
	v_nop
	v_nop
	v_min_u32_e32 v1, v38, v40
	v_min_u32_e32 v0, v39, v41
	v_mfma_f32_16x16x32_f16 v[74:77], v[22:25], v[78:81], v[30:33]
	v_min3_u32 v1, v1, v42, v44
	v_min3_u32 v0, v0, v43, v45
	v_exp_f32_e32 v1, v1
	v_exp_f32_e32 v0, v0
	v_add_f32_e32 v1, 1.0, v1
	v_add_f32_e32 v0, 1.0, v0
	v_rcp_f32_e32 v1, v1
	v_rcp_f32_e32 v0, v0
	v_cvt_pk_f16_f32 v78, v82, v83
	v_cvt_pk_f16_f32 v34, v1, v0
	v_cvt_pk_f16_f32 v79, v84, v85
	v_cvt_pk_f16_f32 v80, v86, v87
	v_mov_b32_dpp v35, v34 quad_perm:[1,2,3,0] row_mask:0xf bank_mask:0xf bound_ctrl:1
	v_mov_b32_dpp v36, v34 quad_perm:[2,3,0,1] row_mask:0xf bank_mask:0xf bound_ctrl:1
	v_mov_b32_dpp v37, v34 quad_perm:[3,0,1,2] row_mask:0xf bank_mask:0xf bound_ctrl:1
	v_cvt_pk_f16_f32 v81, v88, v89
	s_nop 0
	v_mfma_f32_16x16x32_f16 v[38:41], v[2:5], v[34:37], v[62:65]
	v_mfma_f32_16x16x32_f16 v[42:45], v[14:17], v[34:37], v[66:69]
	ds_read_b128 v[82:85], v94 offset:640
	ds_read_b128 v[86:89], v94 offset:656
	v_mfma_f32_16x16x32_f16 v[46:49], v[6:9], v[78:81], v[26:29]
	v_nop
	v_nop
	v_min_u32_e32 v1, v38, v40
	v_min_u32_e32 v0, v39, v41
	v_mfma_f32_16x16x32_f16 v[50:53], v[18:21], v[78:81], v[30:33]
	v_min3_u32 v1, v1, v42, v44
	v_min3_u32 v0, v0, v43, v45
	v_exp_f32_e32 v1, v1
	v_exp_f32_e32 v0, v0
	v_add_f32_e32 v1, 1.0, v1
	v_add_f32_e32 v0, 1.0, v0
	v_rcp_f32_e32 v1, v1
	v_rcp_f32_e32 v0, v0
	v_lshl_add_u64 v[92:93], v[90:91], 0, s[0:1]
	v_cvt_pk_f16_f32 v34, v1, v0
	v_lshl_add_u64 v[96:97], v[90:91], 0, s[2:3]
	v_lshl_add_u64 v[98:99], v[90:91], 0, s[4:5]
	v_mov_b32_dpp v35, v34 quad_perm:[1,2,3,0] row_mask:0xf bank_mask:0xf bound_ctrl:1
	v_mov_b32_dpp v36, v34 quad_perm:[2,3,0,1] row_mask:0xf bank_mask:0xf bound_ctrl:1
	v_mov_b32_dpp v37, v34 quad_perm:[3,0,1,2] row_mask:0xf bank_mask:0xf bound_ctrl:1
	v_lshl_add_u64 v[100:101], v[90:91], 0, s[6:7]
	s_nop 0
	v_mfma_f32_16x16x32_f16 v[38:41], v[2:5], v[34:37], v[70:73]
	v_mfma_f32_16x16x32_f16 v[42:45], v[14:17], v[34:37], v[74:77]
	s_waitcnt lgkmcnt(0)
	v_mfma_f32_16x16x32_f16 v[54:57], v[10:13], v[78:81], v[26:29]
	v_nop
	v_nop
	v_min_u32_e32 v1, v38, v40
	v_min_u32_e32 v0, v39, v41
	v_mfma_f32_16x16x32_f16 v[58:61], v[22:25], v[78:81], v[30:33]
	v_min3_u32 v1, v1, v42, v44
	v_min3_u32 v0, v0, v43, v45
	v_exp_f32_e32 v1, v1
	v_exp_f32_e32 v0, v0
	v_add_f32_e32 v1, 1.0, v1
	v_add_f32_e32 v0, 1.0, v0
	v_rcp_f32_e32 v1, v1
	v_rcp_f32_e32 v0, v0
	v_cvt_pk_f16_f32 v78, v82, v83
	v_cvt_pk_f16_f32 v34, v1, v0
	v_cvt_pk_f16_f32 v79, v84, v85
	v_cvt_pk_f16_f32 v80, v86, v87
	v_mov_b32_dpp v35, v34 quad_perm:[1,2,3,0] row_mask:0xf bank_mask:0xf bound_ctrl:1
	v_mov_b32_dpp v36, v34 quad_perm:[2,3,0,1] row_mask:0xf bank_mask:0xf bound_ctrl:1
	v_mov_b32_dpp v37, v34 quad_perm:[3,0,1,2] row_mask:0xf bank_mask:0xf bound_ctrl:1
	v_cvt_pk_f16_f32 v81, v88, v89
	s_nop 0
	v_mfma_f32_16x16x32_f16 v[38:41], v[2:5], v[34:37], v[46:49]
	v_mfma_f32_16x16x32_f16 v[42:45], v[14:17], v[34:37], v[50:53]
	ds_read_b128 v[82:85], v94 offset:768
	ds_read_b128 v[86:89], v94 offset:784
	v_mfma_f32_16x16x32_f16 v[62:65], v[6:9], v[78:81], v[26:29]
	v_nop
	v_nop
	v_min_u32_e32 v1, v38, v40
	v_min_u32_e32 v0, v39, v41
	v_mfma_f32_16x16x32_f16 v[66:69], v[18:21], v[78:81], v[30:33]
	v_min3_u32 v1, v1, v42, v44
	v_min3_u32 v0, v0, v43, v45
	v_exp_f32_e32 v1, v1
	v_exp_f32_e32 v0, v0
	v_add_f32_e32 v1, 1.0, v1
	v_add_f32_e32 v0, 1.0, v0
	v_rcp_f32_e32 v1, v1
	v_rcp_f32_e32 v0, v0
	s_nop 0
	v_cvt_pk_f16_f32 v34, v1, v0
	s_nop 0
	s_nop 0
	v_mov_b32_dpp v35, v34 quad_perm:[1,2,3,0] row_mask:0xf bank_mask:0xf bound_ctrl:1
	v_mov_b32_dpp v36, v34 quad_perm:[2,3,0,1] row_mask:0xf bank_mask:0xf bound_ctrl:1
	v_mov_b32_dpp v37, v34 quad_perm:[3,0,1,2] row_mask:0xf bank_mask:0xf bound_ctrl:1
	s_nop 0
	s_nop 0
	v_mfma_f32_16x16x32_f16 v[38:41], v[2:5], v[34:37], v[54:57]
	v_mfma_f32_16x16x32_f16 v[42:45], v[14:17], v[34:37], v[58:61]
	s_waitcnt lgkmcnt(0)
	v_mfma_f32_16x16x32_f16 v[70:73], v[10:13], v[78:81], v[26:29]
	v_nop
	v_nop
	v_min_u32_e32 v1, v38, v40
	v_min_u32_e32 v0, v39, v41
	v_mfma_f32_16x16x32_f16 v[74:77], v[22:25], v[78:81], v[30:33]
	v_min3_u32 v1, v1, v42, v44
	v_min3_u32 v0, v0, v43, v45
	v_exp_f32_e32 v1, v1
	v_exp_f32_e32 v0, v0
	v_add_f32_e32 v1, 1.0, v1
	v_add_f32_e32 v0, 1.0, v0
	v_rcp_f32_e32 v1, v1
	v_rcp_f32_e32 v0, v0
	v_cvt_pk_f16_f32 v78, v82, v83
	v_cvt_pk_f16_f32 v34, v1, v0
	v_cvt_pk_f16_f32 v79, v84, v85
	v_cvt_pk_f16_f32 v80, v86, v87
	v_mov_b32_dpp v35, v34 quad_perm:[1,2,3,0] row_mask:0xf bank_mask:0xf bound_ctrl:1
	v_mov_b32_dpp v36, v34 quad_perm:[2,3,0,1] row_mask:0xf bank_mask:0xf bound_ctrl:1
	v_mov_b32_dpp v37, v34 quad_perm:[3,0,1,2] row_mask:0xf bank_mask:0xf bound_ctrl:1
	v_cvt_pk_f16_f32 v81, v88, v89
	s_nop 0
	v_mfma_f32_16x16x32_f16 v[38:41], v[2:5], v[34:37], v[62:65]
	v_mfma_f32_16x16x32_f16 v[42:45], v[14:17], v[34:37], v[66:69]
	ds_read_b128 v[82:85], v94 offset:896
	ds_read_b128 v[86:89], v94 offset:912
	v_mfma_f32_16x16x32_f16 v[46:49], v[6:9], v[78:81], v[26:29]
	v_nop
	v_nop
	v_min_u32_e32 v1, v38, v40
	v_min_u32_e32 v0, v39, v41
	v_mfma_f32_16x16x32_f16 v[50:53], v[18:21], v[78:81], v[30:33]
	v_min3_u32 v1, v1, v42, v44
	v_min3_u32 v0, v0, v43, v45
	v_exp_f32_e32 v1, v1
	v_exp_f32_e32 v0, v0
	v_add_f32_e32 v1, 1.0, v1
	v_add_f32_e32 v0, 1.0, v0
	v_rcp_f32_e32 v1, v1
	v_rcp_f32_e32 v0, v0
	s_nop 0
	v_cvt_pk_f16_f32 v34, v1, v0
	s_nop 0
	s_nop 0
	v_mov_b32_dpp v35, v34 quad_perm:[1,2,3,0] row_mask:0xf bank_mask:0xf bound_ctrl:1
	v_mov_b32_dpp v36, v34 quad_perm:[2,3,0,1] row_mask:0xf bank_mask:0xf bound_ctrl:1
	v_mov_b32_dpp v37, v34 quad_perm:[3,0,1,2] row_mask:0xf bank_mask:0xf bound_ctrl:1
	s_nop 0
	s_nop 0
	v_mfma_f32_16x16x32_f16 v[38:41], v[2:5], v[34:37], v[70:73]
	s_waitcnt vmcnt(8)
	s_cbranch_vccz .Ltail_wait
.Ltail_back:
	s_mov_b32 m0, s9
	v_mfma_f32_16x16x32_f16 v[42:45], v[14:17], v[34:37], v[74:77]
	s_waitcnt lgkmcnt(0)
	v_mfma_f32_16x16x32_f16 v[54:57], v[10:13], v[78:81], v[26:29]
	v_nop
	v_nop
	v_min_u32_e32 v1, v38, v40
	v_min_u32_e32 v0, v39, v41
	v_mfma_f32_16x16x32_f16 v[58:61], v[22:25], v[78:81], v[30:33]
	v_min3_u32 v1, v1, v42, v44
	v_min3_u32 v0, v0, v43, v45
	v_exp_f32_e32 v1, v1
	v_exp_f32_e32 v0, v0
	v_add_f32_e32 v1, 1.0, v1
	v_add_f32_e32 v0, 1.0, v0
	v_rcp_f32_e32 v1, v1
	v_rcp_f32_e32 v0, v0
	v_cvt_pk_f16_f32 v78, v82, v83
	v_cvt_pk_f16_f32 v34, v1, v0
	v_cvt_pk_f16_f32 v79, v84, v85
	v_cvt_pk_f16_f32 v80, v86, v87
	v_mov_b32_dpp v35, v34 quad_perm:[1,2,3,0] row_mask:0xf bank_mask:0xf bound_ctrl:1
	v_mov_b32_dpp v36, v34 quad_perm:[2,3,0,1] row_mask:0xf bank_mask:0xf bound_ctrl:1
	v_mov_b32_dpp v37, v34 quad_perm:[3,0,1,2] row_mask:0xf bank_mask:0xf bound_ctrl:1
	v_cvt_pk_f16_f32 v81, v88, v89
	s_nop 0
	v_mfma_f32_16x16x32_f16 v[38:41], v[2:5], v[34:37], v[46:49]
	s_cbranch_vccz .Lskip_dma12
	global_load_lds_dwordx4 v[92:93], off nt
.Lskip_dma12:
	s_add_i32 m0, s9, 0x440
	v_mfma_f32_16x16x32_f16 v[42:45], v[14:17], v[34:37], v[50:53]
	ds_read_b128 v[82:85], v95
	ds_read_b128 v[86:89], v95 offset:16
	v_mfma_f32_16x16x32_f16 v[62:65], v[6:9], v[78:81], v[26:29]
	v_nop
	v_nop
	v_min_u32_e32 v1, v38, v40
	v_min_u32_e32 v0, v39, v41
	v_mfma_f32_16x16x32_f16 v[66:69], v[18:21], v[78:81], v[30:33]
	v_min3_u32 v1, v1, v42, v44
	v_min3_u32 v0, v0, v43, v45
	v_exp_f32_e32 v1, v1
	v_exp_f32_e32 v0, v0
	v_add_f32_e32 v1, 1.0, v1
	v_add_f32_e32 v0, 1.0, v0
	v_rcp_f32_e32 v1, v1
	v_rcp_f32_e32 v0, v0
	s_nop 0
	v_cvt_pk_f16_f32 v34, v1, v0
	s_nop 0
	s_nop 0
	v_mov_b32_dpp v35, v34 quad_perm:[1,2,3,0] row_mask:0xf bank_mask:0xf bound_ctrl:1
	v_mov_b32_dpp v36, v34 quad_perm:[2,3,0,1] row_mask:0xf bank_mask:0xf bound_ctrl:1
	v_mov_b32_dpp v37, v34 quad_perm:[3,0,1,2] row_mask:0xf bank_mask:0xf bound_ctrl:1
	s_nop 0
	s_nop 0
	v_mfma_f32_16x16x32_f16 v[38:41], v[2:5], v[34:37], v[54:57]
	s_cbranch_vccz .Lskip_dma13
	global_load_lds_dwordx4 v[96:97], off nt
.Lskip_dma13:
	s_add_i32 m0, s9, 0x880
	v_mfma_f32_16x16x32_f16 v[42:45], v[14:17], v[34:37], v[58:61]
	s_waitcnt lgkmcnt(0)
	v_mfma_f32_16x16x32_f16 v[70:73], v[10:13], v[78:81], v[26:29]
	v_nop
	v_nop
	v_min_u32_e32 v1, v38, v40
	v_min_u32_e32 v0, v39, v41
	v_mfma_f32_16x16x32_f16 v[74:77], v[22:25], v[78:81], v[30:33]
	v_min3_u32 v1, v1, v42, v44
	v_min3_u32 v0, v0, v43, v45
	v_exp_f32_e32 v1, v1
	v_exp_f32_e32 v0, v0
	v_add_f32_e32 v1, 1.0, v1
	v_add_f32_e32 v0, 1.0, v0
	v_rcp_f32_e32 v1, v1
	v_rcp_f32_e32 v0, v0
	v_cvt_pk_f16_f32 v78, v82, v83
	v_cvt_pk_f16_f32 v34, v1, v0
	v_cvt_pk_f16_f32 v79, v84, v85
	v_cvt_pk_f16_f32 v80, v86, v87
	v_mov_b32_dpp v35, v34 quad_perm:[1,2,3,0] row_mask:0xf bank_mask:0xf bound_ctrl:1
	v_mov_b32_dpp v36, v34 quad_perm:[2,3,0,1] row_mask:0xf bank_mask:0xf bound_ctrl:1
	v_mov_b32_dpp v37, v34 quad_perm:[3,0,1,2] row_mask:0xf bank_mask:0xf bound_ctrl:1
	v_cvt_pk_f16_f32 v81, v88, v89
	s_nop 0
	v_mfma_f32_16x16x32_f16 v[38:41], v[2:5], v[34:37], v[62:65]
	s_cbranch_vccz .Lskip_dma14
	global_load_lds_dwordx4 v[98:99], off nt
.Lskip_dma14:
	s_add_i32 m0, s9, 0xcc0
	v_mfma_f32_16x16x32_f16 v[42:45], v[14:17], v[34:37], v[66:69]
	ds_read_b128 v[82:85], v95 offset:128
	ds_read_b128 v[86:89], v95 offset:144
	v_mfma_f32_16x16x32_f16 v[46:49], v[6:9], v[78:81], v[26:29]
	v_nop
	v_nop
	v_min_u32_e32 v1, v38, v40
	v_min_u32_e32 v0, v39, v41
	v_mfma_f32_16x16x32_f16 v[50:53], v[18:21], v[78:81], v[30:33]
	v_min3_u32 v1, v1, v42, v44
	v_min3_u32 v0, v0, v43, v45
	v_exp_f32_e32 v1, v1
	v_exp_f32_e32 v0, v0
	v_add_f32_e32 v1, 1.0, v1
	v_add_f32_e32 v0, 1.0, v0
	v_rcp_f32_e32 v1, v1
	v_rcp_f32_e32 v0, v0
	v_mov_b32_e32 v94, v95
	v_cvt_pk_f16_f32 v34, v1, v0
	s_nop 0
	s_nop 0
	v_mov_b32_dpp v35, v34 quad_perm:[1,2,3,0] row_mask:0xf bank_mask:0xf bound_ctrl:1
	v_mov_b32_dpp v36, v34 quad_perm:[2,3,0,1] row_mask:0xf bank_mask:0xf bound_ctrl:1
	v_mov_b32_dpp v37, v34 quad_perm:[3,0,1,2] row_mask:0xf bank_mask:0xf bound_ctrl:1
	s_nop 0
	s_nop 0
	v_mfma_f32_16x16x32_f16 v[38:41], v[2:5], v[34:37], v[70:73]
	s_cbranch_vccz .Lskip_dma15
	global_load_lds_dwordx4 v[100:101], off nt
.Lskip_dma15:
	v_mfma_f32_16x16x32_f16 v[42:45], v[14:17], v[34:37], v[74:77]
	s_waitcnt lgkmcnt(0)
	v_mfma_f32_16x16x32_f16 v[54:57], v[10:13], v[78:81], v[26:29]
	v_nop
	v_nop
	v_min_u32_e32 v1, v38, v40
	v_min_u32_e32 v0, v39, v41
	v_mfma_f32_16x16x32_f16 v[58:61], v[22:25], v[78:81], v[30:33]
	v_min3_u32 v1, v1, v42, v44
	v_min3_u32 v0, v0, v43, v45
	v_exp_f32_e32 v1, v1
	v_exp_f32_e32 v0, v0
	v_add_f32_e32 v1, 1.0, v1
	v_add_f32_e32 v0, 1.0, v0
	v_rcp_f32_e32 v1, v1
	v_rcp_f32_e32 v0, v0
	v_cvt_pk_f16_f32 v78, v82, v83
	v_cvt_pk_f16_f32 v34, v1, v0
	v_cvt_pk_f16_f32 v79, v84, v85
	v_cvt_pk_f16_f32 v80, v86, v87
	v_mov_b32_dpp v35, v34 quad_perm:[1,2,3,0] row_mask:0xf bank_mask:0xf bound_ctrl:1
	v_mov_b32_dpp v36, v34 quad_perm:[2,3,0,1] row_mask:0xf bank_mask:0xf bound_ctrl:1
	v_mov_b32_dpp v37, v34 quad_perm:[3,0,1,2] row_mask:0xf bank_mask:0xf bound_ctrl:1
	v_cvt_pk_f16_f32 v81, v88, v89
	s_nop 0
	s_cmp_eq_u32 s8, 32
	s_cbranch_scc0 .Lchunk_loop
	s_branch .Lepilogue
